# speedup vs baseline: 1.0060x; 1.0060x over previous
_Z13logits_kernelPKDv8_DF16bS1_PKfS3_PDv2_fS5_Pf:
	s_load_dwordx4 s[4:7], s[0:1], 0x0
	s_load_dwordx4 s[12:15], s[0:1], 0x10
	s_load_dwordx4 s[24:27], s[0:1], 0x20
	s_load_dwordx2 s[28:29], s[0:1], 0x30
	s_and_b32 s3, s2, 1
	s_lshl_b32 s3, s3, 3
	s_bfe_u32 s10, s2, 0x30003
	s_or_b32 s10, s10, s3
	s_bfe_u32 s3, s2, 0x20001
	s_lshl_b32 s3, s3, 2
	s_lshr_b32 s8, s2, 6
	s_or_b32 s3, s3, s8
	v_lshrrev_b32_e32 v1, 6, v0
	v_and_b32_e32 v2, 63, v0
	s_movk_i32 s11, 0x3000
	v_lshlrev_b32_e32 v2, 4, v2
	v_and_b32_e32 v5, 31, v0
	v_mad_u32_u24 v2, v1, s11, v2
	v_lshlrev_b32_e32 v5, 2, v5
	s_lshl_b32 s9, s3, 9
	v_add_u32_e32 v3, 0x1000, v2
	v_add_u32_e32 v4, 0x2000, v2
	v_add_u32_e32 v5, s9, v5
	s_mul_i32 s8, s10, 0xc000
	s_mul_i32 s9, s3, 0x30000
	s_waitcnt lgkmcnt(0)
	s_load_dword s22, s[14:15], 0x0
	global_load_dword v248, v5, s[12:13]
	global_load_dword v249, v5, s[12:13] offset:128
	global_load_dword v250, v5, s[12:13] offset:256
	global_load_dword v251, v5, s[12:13] offset:384
	s_add_u32 s4, s4, s8
	s_addc_u32 s5, s5, 0
	s_add_u32 s6, s6, s9
	s_addc_u32 s7, s7, 0
	s_add_u32 s16, s6, 0xc000
	s_addc_u32 s17, s7, 0
	s_add_u32 s18, s6, 0x18000
	s_addc_u32 s19, s7, 0
	s_add_u32 s20, s6, 0x24000
	s_addc_u32 s21, s7, 0
	global_load_dwordx4 v[8:11], v2, s[4:5]
	global_load_dwordx4 v[56:59], v2, s[6:7]
	global_load_dwordx4 v[104:107], v2, s[16:17]
	global_load_dwordx4 v[152:155], v2, s[18:19]
	global_load_dwordx4 v[200:203], v2, s[20:21]
	global_load_dwordx4 v[12:15], v2, s[4:5] offset:1024
	global_load_dwordx4 v[60:63], v2, s[6:7] offset:1024
	global_load_dwordx4 v[108:111], v2, s[16:17] offset:1024
	global_load_dwordx4 v[156:159], v2, s[18:19] offset:1024
	global_load_dwordx4 v[204:207], v2, s[20:21] offset:1024
	global_load_dwordx4 v[16:19], v2, s[4:5] offset:2048
	global_load_dwordx4 v[64:67], v2, s[6:7] offset:2048
	global_load_dwordx4 v[112:115], v2, s[16:17] offset:2048
	global_load_dwordx4 v[160:163], v2, s[18:19] offset:2048
	global_load_dwordx4 v[208:211], v2, s[20:21] offset:2048
	global_load_dwordx4 v[20:23], v2, s[4:5] offset:3072
	global_load_dwordx4 v[68:71], v2, s[6:7] offset:3072
	global_load_dwordx4 v[116:119], v2, s[16:17] offset:3072
	global_load_dwordx4 v[164:167], v2, s[18:19] offset:3072
	global_load_dwordx4 v[212:215], v2, s[20:21] offset:3072
	global_load_dwordx4 v[24:27], v3, s[4:5]
	global_load_dwordx4 v[72:75], v3, s[6:7]
	global_load_dwordx4 v[120:123], v3, s[16:17]
	global_load_dwordx4 v[168:171], v3, s[18:19]
	global_load_dwordx4 v[216:219], v3, s[20:21]
	global_load_dwordx4 v[28:31], v3, s[4:5] offset:1024
	global_load_dwordx4 v[76:79], v3, s[6:7] offset:1024
	global_load_dwordx4 v[124:127], v3, s[16:17] offset:1024
	global_load_dwordx4 v[172:175], v3, s[18:19] offset:1024
	global_load_dwordx4 v[220:223], v3, s[20:21] offset:1024
	global_load_dwordx4 v[32:35], v3, s[4:5] offset:2048
	global_load_dwordx4 v[80:83], v3, s[6:7] offset:2048
	global_load_dwordx4 v[128:131], v3, s[16:17] offset:2048
	global_load_dwordx4 v[176:179], v3, s[18:19] offset:2048
	global_load_dwordx4 v[224:227], v3, s[20:21] offset:2048
	global_load_dwordx4 v[36:39], v3, s[4:5] offset:3072
	global_load_dwordx4 v[84:87], v3, s[6:7] offset:3072
	global_load_dwordx4 v[132:135], v3, s[16:17] offset:3072
	global_load_dwordx4 v[180:183], v3, s[18:19] offset:3072
	global_load_dwordx4 v[228:231], v3, s[20:21] offset:3072
	global_load_dwordx4 v[40:43], v4, s[4:5]
	global_load_dwordx4 v[88:91], v4, s[6:7]
	global_load_dwordx4 v[136:139], v4, s[16:17]
	global_load_dwordx4 v[184:187], v4, s[18:19]
	global_load_dwordx4 v[232:235], v4, s[20:21]
	global_load_dwordx4 v[44:47], v4, s[4:5] offset:1024
	global_load_dwordx4 v[92:95], v4, s[6:7] offset:1024
	global_load_dwordx4 v[140:143], v4, s[16:17] offset:1024
	global_load_dwordx4 v[188:191], v4, s[18:19] offset:1024
	global_load_dwordx4 v[236:239], v4, s[20:21] offset:1024
	global_load_dwordx4 v[48:51], v4, s[4:5] offset:2048
	global_load_dwordx4 v[96:99], v4, s[6:7] offset:2048
	global_load_dwordx4 v[144:147], v4, s[16:17] offset:2048
	global_load_dwordx4 v[192:195], v4, s[18:19] offset:2048
	global_load_dwordx4 v[240:243], v4, s[20:21] offset:2048
	global_load_dwordx4 v[52:55], v4, s[4:5] offset:3072
	global_load_dwordx4 v[100:103], v4, s[6:7] offset:3072
	global_load_dwordx4 v[148:151], v4, s[16:17] offset:3072
	global_load_dwordx4 v[196:199], v4, s[18:19] offset:3072
	global_load_dwordx4 v[244:247], v4, s[20:21] offset:3072
	s_waitcnt vmcnt(58)
	v_mfma_f32_32x32x16_bf16 a[0:15], v[8:11], v[56:59], 0
	s_waitcnt vmcnt(57)
	v_mfma_f32_32x32x16_bf16 a[0:15], v[8:11], v[104:107], a[0:15]
	s_waitcnt vmcnt(56)
	v_mfma_f32_32x32x16_bf16 a[0:15], v[8:11], v[152:155], a[0:15]
	s_waitcnt vmcnt(55)
	v_mfma_f32_32x32x16_bf16 a[0:15], v[8:11], v[200:203], a[0:15]
	s_waitcnt vmcnt(53)
	v_mfma_f32_32x32x16_bf16 a[0:15], v[12:15], v[60:63], a[0:15]
	s_waitcnt vmcnt(52)
	v_mfma_f32_32x32x16_bf16 a[0:15], v[12:15], v[108:111], a[0:15]
	s_waitcnt vmcnt(51)
	v_mfma_f32_32x32x16_bf16 a[0:15], v[12:15], v[156:159], a[0:15]
	s_waitcnt vmcnt(50)
	v_mfma_f32_32x32x16_bf16 a[0:15], v[12:15], v[204:207], a[0:15]
	s_waitcnt vmcnt(48)
	v_mfma_f32_32x32x16_bf16 a[0:15], v[16:19], v[64:67], a[0:15]
	s_waitcnt vmcnt(47)
	v_mfma_f32_32x32x16_bf16 a[0:15], v[16:19], v[112:115], a[0:15]
	s_waitcnt vmcnt(46)
	v_mfma_f32_32x32x16_bf16 a[0:15], v[16:19], v[160:163], a[0:15]
	s_waitcnt vmcnt(45)
	v_mfma_f32_32x32x16_bf16 a[0:15], v[16:19], v[208:211], a[0:15]
	s_waitcnt vmcnt(43)
	v_mfma_f32_32x32x16_bf16 a[0:15], v[20:23], v[68:71], a[0:15]
	s_waitcnt vmcnt(42)
	v_mfma_f32_32x32x16_bf16 a[0:15], v[20:23], v[116:119], a[0:15]
	s_waitcnt vmcnt(41)
	v_mfma_f32_32x32x16_bf16 a[0:15], v[20:23], v[164:167], a[0:15]
	s_waitcnt vmcnt(40)
	v_mfma_f32_32x32x16_bf16 a[0:15], v[20:23], v[212:215], a[0:15]
	s_waitcnt vmcnt(38)
	v_mfma_f32_32x32x16_bf16 a[0:15], v[24:27], v[72:75], a[0:15]
	s_waitcnt vmcnt(37)
	v_mfma_f32_32x32x16_bf16 a[0:15], v[24:27], v[120:123], a[0:15]
	s_waitcnt vmcnt(36)
	v_mfma_f32_32x32x16_bf16 a[0:15], v[24:27], v[168:171], a[0:15]
	s_waitcnt vmcnt(35)
	v_mfma_f32_32x32x16_bf16 a[0:15], v[24:27], v[216:219], a[0:15]
	s_waitcnt vmcnt(33)
	v_mfma_f32_32x32x16_bf16 a[0:15], v[28:31], v[76:79], a[0:15]
	s_waitcnt vmcnt(32)
	v_mfma_f32_32x32x16_bf16 a[0:15], v[28:31], v[124:127], a[0:15]
	s_waitcnt vmcnt(31)
	v_mfma_f32_32x32x16_bf16 a[0:15], v[28:31], v[172:175], a[0:15]
	s_waitcnt vmcnt(30)
	v_mfma_f32_32x32x16_bf16 a[0:15], v[28:31], v[220:223], a[0:15]
	s_waitcnt vmcnt(28)
	v_mfma_f32_32x32x16_bf16 a[0:15], v[32:35], v[80:83], a[0:15]
	s_waitcnt vmcnt(27)
	v_mfma_f32_32x32x16_bf16 a[0:15], v[32:35], v[128:131], a[0:15]
	s_waitcnt vmcnt(26)
	v_mfma_f32_32x32x16_bf16 a[0:15], v[32:35], v[176:179], a[0:15]
	s_waitcnt vmcnt(25)
	v_mfma_f32_32x32x16_bf16 a[0:15], v[32:35], v[224:227], a[0:15]
	s_waitcnt vmcnt(23)
	v_mfma_f32_32x32x16_bf16 a[0:15], v[36:39], v[84:87], a[0:15]
	s_waitcnt vmcnt(22)
	v_mfma_f32_32x32x16_bf16 a[0:15], v[36:39], v[132:135], a[0:15]
	s_waitcnt vmcnt(21)
	v_mfma_f32_32x32x16_bf16 a[0:15], v[36:39], v[180:183], a[0:15]
	s_waitcnt vmcnt(20)
	v_mfma_f32_32x32x16_bf16 a[0:15], v[36:39], v[228:231], a[0:15]
	s_waitcnt vmcnt(18)
	v_mfma_f32_32x32x16_bf16 a[0:15], v[40:43], v[88:91], a[0:15]
	s_waitcnt vmcnt(17)
	v_mfma_f32_32x32x16_bf16 a[0:15], v[40:43], v[136:139], a[0:15]
	s_waitcnt vmcnt(16)
	v_mfma_f32_32x32x16_bf16 a[0:15], v[40:43], v[184:187], a[0:15]
	s_waitcnt vmcnt(15)
	v_mfma_f32_32x32x16_bf16 a[0:15], v[40:43], v[232:235], a[0:15]
	s_waitcnt vmcnt(13)
	v_mfma_f32_32x32x16_bf16 a[0:15], v[44:47], v[92:95], a[0:15]
	s_waitcnt vmcnt(12)
	v_mfma_f32_32x32x16_bf16 a[0:15], v[44:47], v[140:143], a[0:15]
	s_waitcnt vmcnt(11)
	v_mfma_f32_32x32x16_bf16 a[0:15], v[44:47], v[188:191], a[0:15]
	s_waitcnt vmcnt(10)
	v_mfma_f32_32x32x16_bf16 a[0:15], v[44:47], v[236:239], a[0:15]
	v_add_f32_e32 v8, 0, v248
	v_add_f32_e32 v8, v8, v249
	v_add_f32_e32 v8, v8, v250
	v_add_f32_e32 v8, v8, v251
	v_mov_b32_e32 v9, 0x3fb8aa3b
	s_waitcnt lgkmcnt(0)
	v_mul_f32_e32 v9, s22, v9
	v_exp_f32_e32 v9, v9
	v_add_f32_e32 v10, 0x2b8cbccc, v8
	v_div_scale_f32 v11, s[8:9], v10, v10, v9
	v_rcp_f32_e32 v12, v11
	v_div_scale_f32 v13, vcc, v9, v10, v9
	v_fma_f32 v14, -v11, v12, 1.0
	v_fmac_f32_e32 v12, v14, v12
	v_mul_f32_e32 v14, v13, v12
	v_fma_f32 v15, -v11, v14, v13
	v_fmac_f32_e32 v14, v15, v12
	v_fma_f32 v11, -v11, v14, v13
	v_div_fmas_f32 v11, v11, v12, v14
	v_div_fixup_f32 v9, v11, v10, v9
	v_lshlrev_b32_e32 v10, 2, v0
	v_add_u32_e32 v10, 0x4000, v10
	v_cmp_gt_u32_e32 vcc, 32, v0
	s_and_saveexec_b64 s[8:9], vcc
	ds_write2_b32 v10, v8, v9 offset0:128 offset1:160
	s_mov_b64 exec, s[8:9]
	s_waitcnt vmcnt(8)
	v_mfma_f32_32x32x16_bf16 a[0:15], v[48:51], v[96:99], a[0:15]
	s_waitcnt vmcnt(7)
	v_mfma_f32_32x32x16_bf16 a[0:15], v[48:51], v[144:147], a[0:15]
	s_waitcnt vmcnt(6)
	v_mfma_f32_32x32x16_bf16 a[0:15], v[48:51], v[192:195], a[0:15]
	s_waitcnt vmcnt(5)
	v_mfma_f32_32x32x16_bf16 a[0:15], v[48:51], v[240:243], a[0:15]
	v_mul_u32_u24_e32 v1, 0x1080, v1
	s_movk_i32 s4, 0x7f
	s_movk_i32 s6, 0x84
	v_cmp_lt_u32_e32 vcc, s4, v0
	v_lshrrev_b32_e32 v11, 3, v0
	v_and_b32_e32 v10, 31, v0
	v_and_b32_e32 v11, 4, v11
	v_mul_u32_u24_e32 v11, 0x84, v11
	v_lshlrev_b32_e32 v9, 2, v10
	v_bfe_u32 v6, v0, 2, 5
	v_and_b32_e32 v7, 3, v0
	v_add3_u32 v1, v1, v11, v9
	v_lshlrev_b32_e32 v8, 3, v7
	s_waitcnt vmcnt(3)
	v_mfma_f32_32x32x16_bf16 a[0:15], v[52:55], v[100:103], a[0:15]
	s_waitcnt vmcnt(2)
	v_mfma_f32_32x32x16_bf16 a[0:15], v[52:55], v[148:151], a[0:15]
	s_waitcnt vmcnt(1)
	v_mfma_f32_32x32x16_bf16 a[0:15], v[52:55], v[196:199], a[0:15]
	s_waitcnt vmcnt(0)
	v_mfma_f32_32x32x16_bf16 a[0:15], v[52:55], v[244:247], a[0:15]
	s_nop 11
	ds_write_b32 v1, a0
	ds_write_b32 v1, a1 offset:132
	ds_write_b32 v1, a2 offset:264
	ds_write_b32 v1, a3 offset:396
	ds_write_b32 v1, a4 offset:1056
	ds_write_b32 v1, a5 offset:1188
	ds_write_b32 v1, a6 offset:1320
	ds_write_b32 v1, a7 offset:1452
	ds_write_b32 v1, a8 offset:2112
	ds_write_b32 v1, a9 offset:2244
	ds_write_b32 v1, a10 offset:2376
	ds_write_b32 v1, a11 offset:2508
	ds_write_b32 v1, a12 offset:3168
	ds_write_b32 v1, a13 offset:3300
	ds_write_b32 v1, a14 offset:3432
	ds_write_b32 v1, a15 offset:3564
	v_bfe_u32 v6, v0, 2, 5
	v_and_b32_e32 v7, 3, v0
	v_lshlrev_b32_e32 v9, 3, v7
	v_readfirstlane_b32 s30, v0
	v_sub_u32_e32 v10, v6, v9
	s_waitcnt lgkmcnt(0)
	s_barrier
	s_cmpk_ge_u32 s30, 0x80
	s_cbranch_scc1 .Llg_k1
	v_mul_u32_u24_e32 v2, 0x84, v6
	v_lshlrev_b32_e32 v8, 5, v7
	v_add_u32_e32 v2, v2, v8
	v_add_u32_e32 v8, 0x4280, v8
	v_add_u32_e32 v3, 0x1080, v2
	v_add_u32_e32 v4, 0x2100, v2
	v_add_u32_e32 v5, 0x3180, v2
	ds_read_b128 v[48:51], v8
	ds_read_b128 v[52:55], v8 offset:16
	ds_read2_b32 v[16:17], v2 offset0:0 offset1:1
	ds_read2_b32 v[18:19], v2 offset0:2 offset1:3
	ds_read2_b32 v[20:21], v2 offset0:4 offset1:5
	ds_read2_b32 v[22:23], v2 offset0:6 offset1:7
	ds_read2_b32 v[24:25], v3 offset0:0 offset1:1
	ds_read2_b32 v[26:27], v3 offset0:2 offset1:3
	ds_read2_b32 v[28:29], v3 offset0:4 offset1:5
	ds_read2_b32 v[30:31], v3 offset0:6 offset1:7
	ds_read2_b32 v[32:33], v4 offset0:0 offset1:1
	ds_read2_b32 v[34:35], v4 offset0:2 offset1:3
	ds_read2_b32 v[36:37], v4 offset0:4 offset1:5
	ds_read2_b32 v[38:39], v4 offset0:6 offset1:7
	s_waitcnt lgkmcnt(4)
	ds_read2_b32 v[40:41], v5 offset0:0 offset1:1
	ds_read2_b32 v[42:43], v5 offset0:2 offset1:3
	ds_read2_b32 v[44:45], v5 offset0:4 offset1:5
	ds_read2_b32 v[46:47], v5 offset0:6 offset1:7
	s_waitcnt lgkmcnt(0)
	s_branch .Llg_join
